# prepB tiles (second kind): the four serial (S5P, S5BB) load pairs issued together with counted waits
# speedup vs baseline: 1.0098x; 1.0036x over previous
; __device__ __forceinline__ unsigned pk2bf(float lo, float hi) { const f32x2 v = {lo, hi}; return __builtin_bit_cast(unsigned, __builtin_convertvector(v, bf16x2_t)); }
; __device__ __forceinline__ void ph_prepB(const Ctx& c, int tile) {
;     ...
;     else {
;         const int it = (tile - 3072) * NTHR + c.tid;
;         const int ncq = it & 31, kr = (it >> 5) & 511, lg = it >> 14, l = lg >> 4, g = lg & 15;
;         const int s = kr >> 4, cp = kr & 15, d = ncq >> 4, p0 = (ncq & 15) * 4, e = d == 0 ? 31 - s : s;
;         const int ldg = (l * 2 + d) * 16 + g;
;         float v[8];
; #pragma unroll
;         for (int i = 0; i < 4; ++i) {
;             const int p = p0 + i;
;             const float pr = S5P[((size_t)(ldg * 64 + p) * 33 + e) * 2], pi = S5P[((size_t)(ldg * 64 + p) * 33 + e) * 2 + 1];
;             const float br = S5BB[((size_t)(ldg * 64 + p) * 16 + cp) * 2], bi = S5BB[((size_t)(ldg * 64 + p) * 16 + cp) * 2 + 1];
;             v[2 * i] = pr * br - pi * bi; v[2 * i + 1] = pr * bi + pi * br;
;         }
;         u32x4 o; o[0] = pk2bf(v[0], v[1]); o[1] = pk2bf(v[2], v[3]); o[2] = pk2bf(v[4], v[5]); o[3] = pk2bf(v[6], v[7]);
;         *(u32x4*)(WSm + ((size_t)lg * 512 + kr) * 256 + ncq * 8) = o;
;     }
.Lip_noperm:
	s_cmpk_gt_i32 s60, 0x98f
	s_mov_b64 s[0:1], -1
	s_cbranch_scc0 .LBB0_544
	s_load_dwordx2 s[28:29], s[4:5], 0x130
	s_add_i32 s6, s60, 0xfffff670
	v_and_b32_e32 v30, 31, v147
	s_waitcnt lgkmcnt(0)
	s_add_u32 s42, s28, 0x103d4000
	s_addc_u32 s43, s29, 0
	s_cmpk_gt_u32 s6, 0xbff
	s_cbranch_scc0 .LBB0_537
	s_lshl_b32 s0, s6, 8
	s_add_i32 s0, s0, 0xfff40000
	s_waitcnt vmcnt(0)
	v_add_u32_e32 v5, s0, v147
	v_lshrrev_b32_e32 v2, 5, v5
	v_bfe_u32 v2, v2, 4, 5
	v_cmp_gt_u32_e32 vcc, 16, v30
	v_xor_b32_e32 v7, 31, v2
	v_ashrrev_i32_e32 v8, 14, v5
	v_cndmask_b32_e32 v2, v2, v7, vcc
	v_ashrrev_i32_e32 v7, 13, v5
	v_and_b32_e32 v4, 15, v8
	v_lshlrev_b32_e32 v6, 2, v147
	v_and_b32_e32 v7, 0x3ffffe0, v7
	v_and_b32_e32 v9, 16, v147
	v_bfe_u32 v26, v5, 5, 9
	v_and_b32_e32 v6, 60, v6
	v_or3_b32 v4, v9, v7, v4
	v_lshrrev_b32_e32 v5, 2, v5
	v_lshl_or_b32 v4, v4, 6, v6
	v_and_b32_e32 v6, 0x78, v5
	v_mov_b32_e32 v7, v3
	v_lshl_add_u64 v[6:7], s[28:29], 0, v[6:7]
	s_mov_b64 s[0:1], 0x144000
	v_ashrrev_i32_e32 v5, 31, v4
	v_lshl_add_u64 v[6:7], v[6:7], 0, s[0:1]
	v_or_b32_e32 v160, 1, v4
	v_or_b32_e32 v162, 2, v4
	v_or_b32_e32 v164, 3, v4
	v_ashrrev_i32_e32 v161, 31, v160
	v_ashrrev_i32_e32 v163, 31, v162
	v_ashrrev_i32_e32 v165, 31, v164
	v_mad_i64_i32 v[174:175], s[0:1], v4, 33, v[2:3]
	v_mad_i64_i32 v[176:177], s[0:1], v160, 33, v[2:3]
	v_mad_i64_i32 v[178:179], s[0:1], v162, 33, v[2:3]
	v_mad_i64_i32 v[180:181], s[0:1], v164, 33, v[2:3]
	v_lshlrev_b64 v[166:167], 7, v[4:5]
	v_lshlrev_b64 v[168:169], 7, v[160:161]
	v_lshlrev_b64 v[170:171], 7, v[162:163]
	v_lshlrev_b64 v[172:173], 7, v[164:165]
	v_lshl_add_u64 v[174:175], v[174:175], 3, s[42:43]
	v_lshl_add_u64 v[166:167], v[6:7], 0, v[166:167]
	v_lshl_add_u64 v[176:177], v[176:177], 3, s[42:43]
	v_lshl_add_u64 v[168:169], v[6:7], 0, v[168:169]
	v_lshl_add_u64 v[178:179], v[178:179], 3, s[42:43]
	v_lshl_add_u64 v[170:171], v[6:7], 0, v[170:171]
	v_lshl_add_u64 v[180:181], v[180:181], 3, s[42:43]
	v_lshl_add_u64 v[172:173], v[6:7], 0, v[172:173]
	global_load_dwordx2 v[182:183], v[166:167], off
	global_load_dwordx2 v[190:191], v[174:175], off
	global_load_dwordx2 v[184:185], v[168:169], off
	global_load_dwordx2 v[192:193], v[176:177], off
	global_load_dwordx2 v[186:187], v[170:171], off
	global_load_dwordx2 v[194:195], v[178:179], off
	global_load_dwordx2 v[188:189], v[172:173], off
	global_load_dwordx2 v[196:197], v[180:181], off
	v_ashrrev_i32_e32 v9, 31, v8
	v_lshlrev_b64 v[8:9], 18, v[8:9]
	v_lshl_add_u64 v[8:9], s[28:29], 0, v[8:9]
	v_lshlrev_b32_e32 v2, 9, v26
	v_lshl_add_u64 v[8:9], v[8:9], 0, v[2:3]
	v_lshlrev_b32_e32 v2, 4, v30
	v_lshl_add_u64 v[8:9], v[8:9], 0, v[2:3]
	v_add_co_u32_e32 v8, vcc, 0x11edc000, v8
	s_mov_b64 s[0:1], 0
	s_nop 0
	v_addc_co_u32_e32 v9, vcc, 0, v9, vcc
	s_waitcnt vmcnt(6)
	v_pk_mul_f32 v[18:19], v[190:191], v[182:183] op_sel:[1,1] op_sel_hi:[0,1]
	v_pk_fma_f32 v[16:17], v[190:191], v[182:183], v[18:19] neg_lo:[0,0,1] neg_hi:[0,0,1]
	v_pk_fma_f32 v[10:11], v[190:191], v[182:183], v[18:19] op_sel_hi:[1,0,1]
	s_waitcnt vmcnt(4)
	v_pk_mul_f32 v[18:19], v[192:193], v[184:185] op_sel:[1,1] op_sel_hi:[0,1]
	v_pk_fma_f32 v[20:21], v[192:193], v[184:185], v[18:19] neg_lo:[0,0,1] neg_hi:[0,0,1]
	v_pk_fma_f32 v[12:13], v[192:193], v[184:185], v[18:19] op_sel_hi:[1,0,1]
	s_waitcnt vmcnt(2)
	v_pk_mul_f32 v[18:19], v[194:195], v[186:187] op_sel:[1,1] op_sel_hi:[0,1]
	v_pk_fma_f32 v[24:25], v[194:195], v[186:187], v[18:19] neg_lo:[0,0,1] neg_hi:[0,0,1]
	v_pk_fma_f32 v[14:15], v[194:195], v[186:187], v[18:19] op_sel_hi:[1,0,1]
	s_waitcnt vmcnt(0)
	v_pk_mul_f32 v[18:19], v[196:197], v[188:189] op_sel:[1,1] op_sel_hi:[0,1]
	v_pk_fma_f32 v[22:23], v[196:197], v[188:189], v[18:19] neg_lo:[0,0,1] neg_hi:[0,0,1]
	v_pk_fma_f32 v[6:7], v[196:197], v[188:189], v[18:19] op_sel_hi:[1,0,1]
	v_cvt_pk_bf16_f32 v4, v16, v11
	v_cvt_pk_bf16_f32 v5, v20, v13
	v_cvt_pk_bf16_f32 v6, v24, v15
	v_cvt_pk_bf16_f32 v7, v22, v7
	global_store_dwordx4 v[8:9], v[4:7], off
